# MLA: s_nop 7 in front of the row max reduced to s_nop 0 (12 instructions already separate the last QK MFMA from its readers); SB +0 add dropped
# speedup vs baseline: 1.0038x; 1.0038x over previous
; __device__ __forceinline__ unsigned cvt_pk_bf16(float lo, float hi) { unsigned r; asm volatile("v_cvt_pk_bf16_f32 %0, %1, %2" : "=v"(r) : "v"(lo), "v"(hi)); return r; }
; __device__ __forceinline__ float ex2(float x) { return __builtin_amdgcn_exp2f(x); }
; __device__ __forceinline__ f32x16 mfma32(bf16x8 a, bf16x8 b, f32x16 c) { return __builtin_amdgcn_mfma_f32_32x32x16_bf16(a, b, c, 0, 0, 0); }
; __device__ __forceinline__ float swapsum(float m) { auto rr = __builtin_amdgcn_permlane32_swap(__float_as_uint(m), __float_as_uint(m), false, false); return __uint_as_float(rr[0]) + __uint_as_float(rr[1]); }
; __device__ __forceinline__ u32x4 packp(const f32x16& p, int b) { u32x4 w; w.x = cvt_pk_bf16(p[b], p[b + 1]); w.y = cvt_pk_bf16(p[b + 2], p[b + 3]); w.z = cvt_pk_bf16(p[b + 4], p[b + 5]); w.w = cvt_pk_bf16(p[b + 6], p[b + 7]); return w; }
; __device__ __forceinline__ void sb_unit(int b, int h, int qb, const bf16_t* __restrict__ PROJ, bf16_t* OCAT, float* SSQO, ldsp shm, volatile LAS unsigned* FL) {
;     ...
;             for (int r = 0; r < 16; ++r) { tot += l0[r] + l1[r]; z0[r] += l0[r]; z1[r] += l1[r]; }
;             u32x4 lh[4];
; #pragma unroll
;             for (int k = 0; k < 4; ++k)
; #pragma unroll
;                 for (int j = 0; j < 4; ++j) { const float a = (k < 2) ? l0[(k & 1) * 8 + 2 * j] : l1[(k & 1) * 8 + 2 * j], c = (k < 2) ? l0[(k & 1) * 8 + 2 * j + 1] : l1[(k & 1) * 8 + 2 * j + 1];
;                     lh[k][j] = cvt_pk_bf16(a, c); }
;     ...
;             f32x16 x0, x1;
; #pragma unroll
;             for (int r = 0; r < 16; ++r) { x0[r] = Lc; x1[r] = Lc; }
;             x0 = mfma32(Ta, SB_B(lh[0]), x0); x0 = mfma32(Tb, SB_B(lh[1]), x0); x0 = mfma32(Ton, SB_B(lh[2]), x0); x0 = mfma32(Ton, SB_B(lh[3]), x0);
;             x1 = mfma32(Ta, SB_B(lh[2]), x1); x1 = mfma32(Tb, SB_B(lh[3]), x1);
;     ...
; #pragma unroll
;             for (int r = 0; r < 16; ++r) { z0[r] = ex2(z0[r] + x0[r]); z1[r] = ex2(z1[r] + x1[r]); }
;             if (diag) {
; #pragma unroll
;                 for (int r = 0; r < 16; ++r) { const int kk = kb0 + (r & 3) + 8 * (r >> 2); if (kk >= qabs) z0[r] = 0.f; if (kk + 32 >= qabs) z1[r] = 0.f; } }
;             pv(o, vp0 + (step & 3) * VS, packp(z0, 0), packp(z0, 8), packp(z1, 0), packp(z1, 8));
;             Lc += swapsum(tot);
;             wfin = __all(Lc <= SB_DONE) != 0;
.LBB0_1060:
	v_add_f32_e32 v2, v2, v52
	v_add_f32_e32 v1, v1, v53
	v_add_f32_e32 v52, v54, v56
	v_add_f32_e32 v1, v1, v2
	v_add_f32_e32 v53, v55, v57
	v_add_f32_e32 v1, v52, v1
	v_add_f32_e32 v54, v58, v60
	v_add_f32_e32 v1, v53, v1
	v_add_f32_e32 v55, v59, v61
	v_add_f32_e32 v1, v54, v1
	v_add_f32_e32 v56, v62, v64
	v_add_f32_e32 v1, v55, v1
	v_add_f32_e32 v57, v63, v65
	v_add_f32_e32 v1, v56, v1
	v_add_f32_e32 v58, v66, v68
	v_add_f32_e32 v1, v57, v1
	v_add_f32_e32 v59, v67, v69
	v_add_f32_e32 v1, v58, v1
	v_add_f32_e32 v60, v70, v72
	v_add_f32_e32 v1, v59, v1
	v_add_f32_e32 v61, v71, v73
	v_add_f32_e32 v1, v60, v1
	v_add_f32_e32 v62, v74, v76
	v_add_f32_e32 v1, v61, v1
	v_add_f32_e32 v63, v75, v77
	v_add_f32_e32 v1, v62, v1
	v_add_f32_e32 v64, v78, v80
	v_add_f32_e32 v1, v63, v1
	v_add_f32_e32 v65, v79, v81
	v_add_f32_e32 v1, v64, v1
	v_add_u32_e32 v2, s8, v162
	v_add_f32_e32 v1, v65, v1
	v_cvt_pk_bf16_f32 v56, v84, v83
	v_cvt_pk_bf16_f32 v57, v88, v87
	v_cvt_pk_bf16_f32 v58, v92, v91
	v_cvt_pk_bf16_f32 v59, v96, v95
	v_cvt_pk_bf16_f32 v60, v86, v85
	v_cvt_pk_bf16_f32 v61, v90, v89
	v_cvt_pk_bf16_f32 v62, v94, v93
	v_cvt_pk_bf16_f32 v63, v98, v97
	v_cvt_pk_bf16_f32 v52, v38, v37
	v_cvt_pk_bf16_f32 v53, v42, v41
	v_cvt_pk_bf16_f32 v54, v46, v45
	v_cvt_pk_bf16_f32 v55, v50, v49
	v_cvt_pk_bf16_f32 v38, v40, v39
	v_cvt_pk_bf16_f32 v39, v44, v43
	v_cvt_pk_bf16_f32 v40, v48, v47
	v_cvt_pk_bf16_f32 v41, v82, v51
	ds_read_b64_tr_b16 v[42:43], v2 offset:32768
	ds_read_b64_tr_b16 v[44:45], v2 offset:33280
	ds_read_b64_tr_b16 v[46:47], v2 offset:33792
	ds_read_b64_tr_b16 v[48:49], v2 offset:34304
	ds_read_b64_tr_b16 v[64:65], v2 offset:34816
	ds_read_b64_tr_b16 v[66:67], v2 offset:35328
	ds_read_b64_tr_b16 v[68:69], v2 offset:35840
	ds_read_b64_tr_b16 v[70:71], v2 offset:36352
	s_waitcnt lgkmcnt(0)
	v_mfma_f32_32x32x16_bf16 v[20:35], v[56:59], v[42:45], v[20:35]
	s_mov_b32 s0, 0x43160000
	s_movk_i32 s80, 0xff
	s_mov_b32 s81, 0x41000000
	s_mov_b64 s[82:83], 0x800
	s_mov_b64 s[84:85], 0xc00
	s_mov_b64 s[86:87], 0x70000
	s_mov_b64 s[88:89], 0x70080
	v_mfma_f32_32x32x16_bf16 v[20:35], v[60:63], v[46:49], v[20:35]
	v_mfma_f32_32x32x16_bf16 v[20:35], v[52:55], v[64:67], v[20:35]
	v_mfma_f32_32x32x16_bf16 v[20:35], v[38:41], v[68:71], v[20:35]
	ds_read_b64_tr_b16 v[42:43], v2 offset:36864
	ds_read_b64_tr_b16 v[44:45], v2 offset:37376
	ds_read_b64_tr_b16 v[46:47], v2 offset:37888
	ds_read_b64_tr_b16 v[48:49], v2 offset:38400
	ds_read_b64_tr_b16 v[64:65], v2 offset:38912
	ds_read_b64_tr_b16 v[66:67], v2 offset:39424
	ds_read_b64_tr_b16 v[68:69], v2 offset:39936
	ds_read_b64_tr_b16 v[70:71], v2 offset:40448
	v_mov_b32_e32 v2, v1
	s_nop 1
	v_permlane32_swap_b32_e32 v1, v2
	v_add_f32_e32 v1, v1, v2
	v_add_f32_e32 v36, v36, v1
	v_cmp_le_f32_e32 vcc, s0, v36
	s_waitcnt lgkmcnt(0)
	v_mfma_f32_32x32x16_bf16 v[4:19], v[56:59], v[42:45], v[4:19]
	s_cmp_eq_u64 vcc, exec
	s_cselect_b64 s[0:1], -1, 0
	v_mfma_f32_32x32x16_bf16 v[4:19], v[60:63], v[46:49], v[4:19]
	v_mfma_f32_32x32x16_bf16 v[4:19], v[52:55], v[64:67], v[4:19]
	v_mfma_f32_32x32x16_bf16 v[4:19], v[38:41], v[68:71], v[4:19]

.LBB0_1152:
	s_nop 0
	v_max_f32_e32 v64, v101, v100
	v_max3_f32 v65, v102, v103, v85
	v_max3_f32 v64, v64, v84, v86
	v_max3_f32 v64, v64, v87, v104
	v_max3_f32 v65, v65, v106, v107
	v_max3_f32 v64, v64, v105, v88
	v_max3_f32 v65, v65, v90, v91
	v_max3_f32 v64, v64, v89, v108
	v_max3_f32 v65, v65, v110, v111
	v_max3_f32 v64, v64, v109, v92
	v_max3_f32 v65, v65, v94, v95
	v_max3_f32 v64, v64, v93, v112
	v_max3_f32 v65, v65, v114, v115
	v_max3_f32 v64, v64, v113, v96
	v_max3_f32 v65, v65, v98, v99
	v_max3_f32 v64, v64, v97, v65
	v_mov_b32_e32 v65, v64
	s_nop 1
	v_permlane32_swap_b32_e32 v64, v65
	v_max_f32_e32 v64, v64, v65
	v_cmp_lt_f32_e32 vcc, s81, v64
	s_cmp_lg_u64 vcc, 0
	v_add_f32_e32 v189, v189, v156
	s_cselect_b64 s[10:11], -1, 0
	s_cbranch_vccnz .LBB0_1168

.LBB0_1162:
	s_nop 0
	v_max_f32_e32 v96, v69, v68
	v_max3_f32 v97, v70, v71, v53
	v_max3_f32 v96, v96, v52, v54
	v_max3_f32 v96, v96, v55, v72
	v_max3_f32 v97, v97, v74, v75
	v_max3_f32 v96, v96, v73, v56
	v_max3_f32 v97, v97, v58, v59
	v_max3_f32 v96, v96, v57, v76
	v_max3_f32 v97, v97, v78, v79
	v_max3_f32 v96, v96, v77, v60
	v_max3_f32 v97, v97, v62, v63
	v_max3_f32 v96, v96, v61, v80
	v_max3_f32 v97, v97, v82, v83
	v_max3_f32 v96, v96, v81, v64
	v_max3_f32 v97, v97, v66, v67
	v_max3_f32 v96, v96, v65, v97
	v_mov_b32_e32 v97, v96
	s_nop 1
	v_permlane32_swap_b32_e32 v96, v97
	v_max_f32_e32 v96, v96, v97
	v_cmp_lt_f32_e32 vcc, s81, v96
	s_cmp_lg_u64 vcc, 0
	v_add_f32_e32 v189, v189, v140
	s_cselect_b64 s[10:11], -1, 0
	s_cbranch_vccnz .LBB0_1172
